# row-epilogue gain fragments (attention subln_g, S5 and SGU mix_norm_g) loaded together once instead of one-by-one behind vmcnt(0)
# speedup vs baseline: 1.0247x; 1.0076x over previous
; __device__ __forceinline__ unsigned cvt_pk_bf16(float lo, float hi) { typedef __bf16 bf16x2_t __attribute__((ext_vector_type(2))); f32x2 v = {lo, hi}; bf16x2_t b = __builtin_convertvector(v, bf16x2_t); return __builtin_bit_cast(unsigned, b); }
; __device__ __forceinline__ void sgu_block(const Frame& F, const bf16* __restrict__ proj, const float* lng, const float* lnb, const bf16* __restrict__ wsb, const float* sb, const float* mixg, bf16* mix, int blk) {
;     ...
; #pragma unroll
;     for (int it = 0; it < 2; ++it) { const int i = 64 * ih + 32 * it + r32;
;         const float tot = (red[i] + red[128 + i]) + (red[256 + i] + red[384 + i]);
;         const float rstd = rsqrtf(tot * (1.0f / 512.0f) + EPS);
;         bf16* orow = mix + (size_t)(t0 + i) * D + 1024 + h * 128 + 4 * hi; const float* gp = mixg + h * 128 + 4 * hi;
; #pragma unroll
;         for (int ct = 0; ct < 4; ++ct)
; #pragma unroll
;             for (int rq = 0; rq < 4; ++rq) { const f32x4 gq = *(const f32x4*)(gp + 32 * ct + 8 * rq);
;                 u32x2 wv; wv.x = gm::cvt_pk_bf16(acc[ct][it][4 * rq + 0] * rstd * gq.x, acc[ct][it][4 * rq + 1] * rstd * gq.y); wv.y = gm::cvt_pk_bf16(acc[ct][it][4 * rq + 2] * rstd * gq.z, acc[ct][it][4 * rq + 3] * rstd * gq.w);
;                 *(u32x2*)(orow + 32 * ct + 8 * rq) = wv; } }
.LBB0_436:
	s_or_b64 exec, exec, s[4:5]
	s_add_i32 s4, 0, 0x20000
	v_lshl_add_u32 v138, v192, 2, s4
	s_waitcnt lgkmcnt(0)
	s_barrier
	ds_read2st64_b32 v[136:137], v138 offset1:2
	ds_read2st64_b32 v[138:139], v138 offset0:4 offset1:6
	v_lshl_add_u64 v[134:135], v[128:129], 2, s[86:87]
	v_ashrrev_i32_e32 v131, 31, v130
	v_lshlrev_b64 v[130:131], 12, v[130:131]
	s_waitcnt lgkmcnt(1)
	v_mov_b32_e32 v140, v136
	s_waitcnt lgkmcnt(0)
	v_mov_b32_e32 v141, v138
	v_mov_b32_e32 v138, v137
	v_pk_add_f32 v[136:137], v[140:141], v[138:139]
	global_load_dwordx4 v[144:147], v[134:135], off
	global_load_dwordx4 v[148:151], v[134:135], off offset:32
	global_load_dwordx4 v[152:155], v[134:135], off offset:64
	global_load_dwordx4 v[156:159], v[134:135], off offset:96
	global_load_dwordx4 v[160:163], v[134:135], off offset:128
	global_load_dwordx4 v[164:167], v[134:135], off offset:160
	global_load_dwordx4 v[168:171], v[134:135], off offset:192
	global_load_dwordx4 v[172:175], v[134:135], off offset:224
	global_load_dwordx4 v[176:179], v[134:135], off offset:256
	global_load_dwordx4 v[180:183], v[134:135], off offset:288
	global_load_dwordx4 v[184:187], v[134:135], off offset:320
	global_load_dwordx4 v[188:191], v[134:135], off offset:352
	global_load_dwordx4 v[196:199], v[134:135], off offset:384
	global_load_dwordx4 v[200:203], v[134:135], off offset:416
	global_load_dwordx4 v[204:207], v[134:135], off offset:448
	global_load_dwordx4 v[212:215], v[134:135], off offset:480
	v_add_f32_e32 v136, v136, v137
	v_fmamk_f32 v136, v136, 0x3b000000, v194
	v_cmp_gt_f32_e32 vcc, s26, v136
	v_mul_f32_e32 v137, 0x4b800000, v136
	v_lshl_add_u64 v[130:131], s[88:89], 0, v[130:131]
	v_cndmask_b32_e32 v136, v136, v137, vcc
	v_rsq_f32_e32 v136, v136
	v_lshlrev_b64 v[128:129], 1, v[128:129]
	v_lshl_add_u64 v[130:131], v[130:131], 0, v[128:129]
	v_ashrrev_i32_e32 v79, 31, v78
	v_mul_f32_e32 v137, 0x45800000, v136
	v_cndmask_b32_e32 v136, v136, v137, vcc
	v_pk_mul_f32 v[114:115], v[114:115], v[136:137] op_sel_hi:[1,0]
	v_pk_mul_f32 v[112:113], v[112:113], v[136:137] op_sel_hi:[1,0]
	v_pk_mul_f32 v[132:133], v[132:133], v[136:137] op_sel_hi:[1,0]
	v_pk_mul_f32 v[116:117], v[116:117], v[136:137] op_sel_hi:[1,0]
	v_pk_mul_f32 v[96:97], v[96:97], v[136:137] op_sel_hi:[1,0]
	v_pk_mul_f32 v[98:99], v[98:99], v[136:137] op_sel_hi:[1,0]
	v_pk_mul_f32 v[80:81], v[80:81], v[136:137] op_sel_hi:[1,0]
	v_pk_mul_f32 v[82:83], v[82:83], v[136:137] op_sel_hi:[1,0]
	v_pk_mul_f32 v[64:65], v[64:65], v[136:137] op_sel_hi:[1,0]
	v_pk_mul_f32 v[66:67], v[66:67], v[136:137] op_sel_hi:[1,0]
	s_add_i32 s2, s2, s9
	s_cmpk_lt_i32 s2, 0x80
	s_waitcnt vmcnt(15)
	v_mov_b64_e32 v[138:139], v[144:145]
	v_mov_b64_e32 v[140:141], v[146:147]
	v_pk_mul_f32 v[114:115], v[138:139], v[114:115]
	v_pk_mul_f32 v[112:113], v[140:141], v[112:113]
	v_cvt_pk_bf16_f32 v114, v114, v115
	v_cvt_pk_bf16_f32 v115, v112, v113
	global_store_dwordx2 v[130:131], v[114:115], off offset:2048
	s_waitcnt vmcnt(15)
	v_mov_b64_e32 v[112:113], v[148:149]
	v_mov_b64_e32 v[114:115], v[150:151]
	v_pk_mul_f32 v[112:113], v[112:113], v[132:133]
	v_pk_mul_f32 v[114:115], v[114:115], v[116:117]
	v_cvt_pk_bf16_f32 v112, v112, v113
	v_cvt_pk_bf16_f32 v113, v114, v115
	global_store_dwordx2 v[130:131], v[112:113], off offset:2064
	v_pk_mul_f32 v[116:117], v[120:121], v[136:137] op_sel_hi:[1,0]
	s_waitcnt vmcnt(15)
	v_mov_b64_e32 v[112:113], v[152:153]
	v_mov_b64_e32 v[114:115], v[154:155]
	v_pk_mul_f32 v[112:113], v[112:113], v[116:117]
	v_pk_mul_f32 v[116:117], v[118:119], v[136:137] op_sel_hi:[1,0]
	v_cvt_pk_bf16_f32 v112, v112, v113
	v_pk_mul_f32 v[114:115], v[114:115], v[116:117]
	v_pk_mul_f32 v[116:117], v[124:125], v[136:137] op_sel_hi:[1,0]
	v_cvt_pk_bf16_f32 v113, v114, v115
	global_store_dwordx2 v[130:131], v[112:113], off offset:2080
	s_waitcnt vmcnt(15)
	v_mov_b64_e32 v[112:113], v[156:157]
	v_mov_b64_e32 v[114:115], v[158:159]
	v_pk_mul_f32 v[112:113], v[112:113], v[116:117]
	v_pk_mul_f32 v[116:117], v[122:123], v[136:137] op_sel_hi:[1,0]
	v_cvt_pk_bf16_f32 v112, v112, v113
	v_pk_mul_f32 v[114:115], v[114:115], v[116:117]
	v_pk_mul_f32 v[116:117], v[126:127], v[136:137] op_sel_hi:[1,0]
	v_cvt_pk_bf16_f32 v113, v114, v115
	global_store_dwordx2 v[130:131], v[112:113], off offset:2096
	s_waitcnt vmcnt(15)
	v_mov_b64_e32 v[112:113], v[160:161]
	v_mov_b64_e32 v[114:115], v[162:163]
	v_pk_mul_f32 v[112:113], v[112:113], v[116:117]
	v_pk_mul_f32 v[96:97], v[114:115], v[96:97]
	v_cvt_pk_bf16_f32 v112, v112, v113
	v_cvt_pk_bf16_f32 v113, v96, v97
	global_store_dwordx2 v[130:131], v[112:113], off offset:2112
	v_pk_mul_f32 v[96:97], v[100:101], v[136:137] op_sel_hi:[1,0]
	v_pk_mul_f32 v[100:101], v[104:105], v[136:137] op_sel_hi:[1,0]
	s_waitcnt vmcnt(15)
	v_mov_b64_e32 v[112:113], v[164:165]
	v_mov_b64_e32 v[114:115], v[166:167]
	v_pk_mul_f32 v[96:97], v[96:97], v[112:113]
	v_pk_mul_f32 v[98:99], v[98:99], v[114:115]
	v_cvt_pk_bf16_f32 v96, v96, v97
	v_cvt_pk_bf16_f32 v97, v98, v99
	global_store_dwordx2 v[130:131], v[96:97], off offset:2128
	s_waitcnt vmcnt(15)
	v_mov_b64_e32 v[96:97], v[168:169]
	v_mov_b64_e32 v[98:99], v[170:171]
	v_pk_mul_f32 v[96:97], v[100:101], v[96:97]
	v_pk_mul_f32 v[100:101], v[102:103], v[136:137] op_sel_hi:[1,0]
	v_cvt_pk_bf16_f32 v96, v96, v97
	v_pk_mul_f32 v[98:99], v[100:101], v[98:99]
	v_pk_mul_f32 v[100:101], v[108:109], v[136:137] op_sel_hi:[1,0]
	v_cvt_pk_bf16_f32 v97, v98, v99
	global_store_dwordx2 v[130:131], v[96:97], off offset:2144
	s_waitcnt vmcnt(15)
; __device__ __forceinline__ unsigned cvt_pk_bf16(float lo, float hi) { typedef __bf16 bf16x2_t __attribute__((ext_vector_type(2))); f32x2 v = {lo, hi}; bf16x2_t b = __builtin_convertvector(v, bf16x2_t); return __builtin_bit_cast(unsigned, b); }
; __device__ __forceinline__ void sgu_block(const Frame& F, const bf16* __restrict__ proj, const float* lng, const float* lnb, const bf16* __restrict__ wsb, const float* sb, const float* mixg, bf16* mix, int blk) {
;     ...
; #pragma unroll
;         for (int ct = 0; ct < 4; ++ct)
; #pragma unroll
;             for (int rq = 0; rq < 4; ++rq) { const f32x4 gq = *(const f32x4*)(gp + 32 * ct + 8 * rq);
;                 u32x2 wv; wv.x = gm::cvt_pk_bf16(acc[ct][it][4 * rq + 0] * rstd * gq.x, acc[ct][it][4 * rq + 1] * rstd * gq.y); wv.y = gm::cvt_pk_bf16(acc[ct][it][4 * rq + 2] * rstd * gq.z, acc[ct][it][4 * rq + 3] * rstd * gq.w);
;                 *(u32x2*)(orow + 32 * ct + 8 * rq) = wv; } }
	v_mov_b64_e32 v[96:97], v[172:173]
	v_mov_b64_e32 v[98:99], v[174:175]
	v_pk_mul_f32 v[96:97], v[100:101], v[96:97]
	v_pk_mul_f32 v[100:101], v[106:107], v[136:137] op_sel_hi:[1,0]
	v_cvt_pk_bf16_f32 v96, v96, v97
	v_pk_mul_f32 v[98:99], v[100:101], v[98:99]
	v_pk_mul_f32 v[100:101], v[110:111], v[136:137] op_sel_hi:[1,0]
	v_cvt_pk_bf16_f32 v97, v98, v99
	global_store_dwordx2 v[130:131], v[96:97], off offset:2160
	s_waitcnt vmcnt(15)
	v_mov_b64_e32 v[96:97], v[176:177]
	v_mov_b64_e32 v[98:99], v[178:179]
	v_pk_mul_f32 v[96:97], v[100:101], v[96:97]
	v_pk_mul_f32 v[80:81], v[80:81], v[98:99]
	v_cvt_pk_bf16_f32 v96, v96, v97
	v_cvt_pk_bf16_f32 v97, v80, v81
	global_store_dwordx2 v[130:131], v[96:97], off offset:2176
	v_pk_mul_f32 v[80:81], v[84:85], v[136:137] op_sel_hi:[1,0]
	v_pk_mul_f32 v[84:85], v[88:89], v[136:137] op_sel_hi:[1,0]
	s_waitcnt vmcnt(15)
	v_mov_b64_e32 v[96:97], v[180:181]
	v_mov_b64_e32 v[98:99], v[182:183]
	v_pk_mul_f32 v[80:81], v[80:81], v[96:97]
	v_pk_mul_f32 v[82:83], v[82:83], v[98:99]
	v_cvt_pk_bf16_f32 v80, v80, v81
	v_cvt_pk_bf16_f32 v81, v82, v83
	global_store_dwordx2 v[130:131], v[80:81], off offset:2192
	s_waitcnt vmcnt(15)
	v_mov_b64_e32 v[80:81], v[184:185]
	v_mov_b64_e32 v[82:83], v[186:187]
	v_pk_mul_f32 v[80:81], v[84:85], v[80:81]
	v_pk_mul_f32 v[84:85], v[86:87], v[136:137] op_sel_hi:[1,0]
	v_cvt_pk_bf16_f32 v80, v80, v81
	v_pk_mul_f32 v[82:83], v[84:85], v[82:83]
	v_pk_mul_f32 v[84:85], v[92:93], v[136:137] op_sel_hi:[1,0]
	v_cvt_pk_bf16_f32 v81, v82, v83
	global_store_dwordx2 v[130:131], v[80:81], off offset:2208
	s_waitcnt vmcnt(15)
	v_mov_b64_e32 v[80:81], v[188:189]
	v_mov_b64_e32 v[82:83], v[190:191]
	v_pk_mul_f32 v[80:81], v[84:85], v[80:81]
	v_pk_mul_f32 v[84:85], v[90:91], v[136:137] op_sel_hi:[1,0]
	v_cvt_pk_bf16_f32 v80, v80, v81
	v_pk_mul_f32 v[82:83], v[84:85], v[82:83]
	v_pk_mul_f32 v[84:85], v[94:95], v[136:137] op_sel_hi:[1,0]
	v_cvt_pk_bf16_f32 v81, v82, v83
	global_store_dwordx2 v[130:131], v[80:81], off offset:2224
	s_waitcnt vmcnt(15)
	v_mov_b64_e32 v[80:81], v[196:197]
	v_mov_b64_e32 v[82:83], v[198:199]
	v_pk_mul_f32 v[80:81], v[84:85], v[80:81]
	v_pk_mul_f32 v[64:65], v[64:65], v[82:83]
	v_cvt_pk_bf16_f32 v80, v80, v81
	v_cvt_pk_bf16_f32 v81, v64, v65
	global_store_dwordx2 v[130:131], v[80:81], off offset:2240
	v_pk_mul_f32 v[64:65], v[68:69], v[136:137] op_sel_hi:[1,0]
	v_pk_mul_f32 v[68:69], v[72:73], v[136:137] op_sel_hi:[1,0]
	s_waitcnt vmcnt(15)
	v_mov_b64_e32 v[80:81], v[200:201]
	v_mov_b64_e32 v[82:83], v[202:203]
	v_pk_mul_f32 v[64:65], v[64:65], v[80:81]
	v_pk_mul_f32 v[66:67], v[66:67], v[82:83]
	v_cvt_pk_bf16_f32 v64, v64, v65
	v_cvt_pk_bf16_f32 v65, v66, v67
	global_store_dwordx2 v[130:131], v[64:65], off offset:2256
	s_waitcnt vmcnt(15)
	v_mov_b64_e32 v[64:65], v[204:205]
	v_mov_b64_e32 v[66:67], v[206:207]
	v_pk_mul_f32 v[64:65], v[68:69], v[64:65]
	v_pk_mul_f32 v[68:69], v[70:71], v[136:137] op_sel_hi:[1,0]
	v_cvt_pk_bf16_f32 v64, v64, v65
	v_pk_mul_f32 v[66:67], v[68:69], v[66:67]
	v_pk_mul_f32 v[68:69], v[76:77], v[136:137] op_sel_hi:[1,0]
	v_cvt_pk_bf16_f32 v65, v66, v67
	global_store_dwordx2 v[130:131], v[64:65], off offset:2272
	s_waitcnt vmcnt(15)
	v_mov_b64_e32 v[64:65], v[212:213]
	v_mov_b64_e32 v[66:67], v[214:215]
	v_pk_mul_f32 v[64:65], v[68:69], v[64:65]
	v_pk_mul_f32 v[68:69], v[74:75], v[136:137] op_sel_hi:[1,0]
	v_cvt_pk_bf16_f32 v64, v64, v65
	v_pk_mul_f32 v[66:67], v[68:69], v[66:67]
	s_nop 0
	v_cvt_pk_bf16_f32 v65, v66, v67
	global_store_dwordx2 v[130:131], v[64:65], off offset:2288
	v_lshl_add_u32 v66, v210, 2, s4
	ds_read2st64_b32 v[64:65], v66 offset1:2
	ds_read2st64_b32 v[66:67], v66 offset0:4 offset1:6
	s_waitcnt lgkmcnt(1)
	v_mov_b32_e32 v68, v64
	s_waitcnt lgkmcnt(0)
; __device__ __forceinline__ unsigned cvt_pk_bf16(float lo, float hi) { typedef __bf16 bf16x2_t __attribute__((ext_vector_type(2))); f32x2 v = {lo, hi}; bf16x2_t b = __builtin_convertvector(v, bf16x2_t); return __builtin_bit_cast(unsigned, b); }
; __device__ __forceinline__ void sgu_block(const Frame& F, const bf16* __restrict__ proj, const float* lng, const float* lnb, const bf16* __restrict__ wsb, const float* sb, const float* mixg, bf16* mix, int blk) {
;     ...
; #pragma unroll
;     for (int it = 0; it < 2; ++it) { const int i = 64 * ih + 32 * it + r32;
;         const float tot = (red[i] + red[128 + i]) + (red[256 + i] + red[384 + i]);
;         const float rstd = rsqrtf(tot * (1.0f / 512.0f) + EPS);
;         bf16* orow = mix + (size_t)(t0 + i) * D + 1024 + h * 128 + 4 * hi; const float* gp = mixg + h * 128 + 4 * hi;
; #pragma unroll
;         for (int ct = 0; ct < 4; ++ct)
; #pragma unroll
;             for (int rq = 0; rq < 4; ++rq) { const f32x4 gq = *(const f32x4*)(gp + 32 * ct + 8 * rq);
;                 u32x2 wv; wv.x = gm::cvt_pk_bf16(acc[ct][it][4 * rq + 0] * rstd * gq.x, acc[ct][it][4 * rq + 1] * rstd * gq.y); wv.y = gm::cvt_pk_bf16(acc[ct][it][4 * rq + 2] * rstd * gq.z, acc[ct][it][4 * rq + 3] * rstd * gq.w);
;                 *(u32x2*)(orow + 32 * ct + 8 * rq) = wv; } }
	v_mov_b32_e32 v69, v66
	v_mov_b32_e32 v66, v65
	v_pk_add_f32 v[64:65], v[68:69], v[66:67]
	v_add_f32_e32 v64, v64, v65
	v_fmamk_f32 v64, v64, 0x3b000000, v194
	v_cmp_gt_f32_e32 vcc, s26, v64
	v_mul_f32_e32 v65, 0x4b800000, v64
	s_nop 0
	v_cndmask_b32_e32 v64, v64, v65, vcc
	v_rsq_f32_e32 v64, v64
	s_nop 0
	v_mul_f32_e32 v65, 0x45800000, v64
	v_cndmask_b32_e32 v66, v64, v65, vcc
	v_lshlrev_b64 v[64:65], 12, v[78:79]
	v_pk_mul_f32 v[48:49], v[48:49], v[66:67] op_sel_hi:[1,0]
	v_pk_mul_f32 v[50:51], v[50:51], v[66:67] op_sel_hi:[1,0]
	v_lshl_add_u64 v[64:65], s[88:89], 0, v[64:65]
	v_lshl_add_u64 v[64:65], v[64:65], 0, v[128:129]
	v_pk_mul_f32 v[52:53], v[52:53], v[66:67] op_sel_hi:[1,0]
	v_pk_mul_f32 v[32:33], v[32:33], v[66:67] op_sel_hi:[1,0]
	v_pk_mul_f32 v[34:35], v[34:35], v[66:67] op_sel_hi:[1,0]
	v_pk_mul_f32 v[36:37], v[36:37], v[66:67] op_sel_hi:[1,0]
	v_pk_mul_f32 v[16:17], v[16:17], v[66:67] op_sel_hi:[1,0]
	v_pk_mul_f32 v[18:19], v[18:19], v[66:67] op_sel_hi:[1,0]
	v_pk_mul_f32 v[20:21], v[20:21], v[66:67] op_sel_hi:[1,0]
	v_pk_mul_f32 v[0:1], v[0:1], v[66:67] op_sel_hi:[1,0]
	v_pk_mul_f32 v[2:3], v[2:3], v[66:67] op_sel_hi:[1,0]
	v_pk_mul_f32 v[4:5], v[4:5], v[66:67] op_sel_hi:[1,0]
	v_mov_b64_e32 v[68:69], v[144:145]
	v_mov_b64_e32 v[70:71], v[146:147]
	v_pk_mul_f32 v[48:49], v[68:69], v[48:49]
	v_pk_mul_f32 v[50:51], v[70:71], v[50:51]
	v_cvt_pk_bf16_f32 v48, v48, v49
	v_cvt_pk_bf16_f32 v49, v50, v51
	global_store_dwordx2 v[64:65], v[48:49], off offset:2048
	v_mov_b64_e32 v[48:49], v[148:149]
	v_mov_b64_e32 v[50:51], v[150:151]
	v_pk_mul_f32 v[48:49], v[48:49], v[52:53]
	v_pk_mul_f32 v[52:53], v[54:55], v[66:67] op_sel_hi:[1,0]
	v_cvt_pk_bf16_f32 v48, v48, v49
	v_pk_mul_f32 v[50:51], v[50:51], v[52:53]
	v_pk_mul_f32 v[52:53], v[56:57], v[66:67] op_sel_hi:[1,0]
	v_cvt_pk_bf16_f32 v49, v50, v51
	global_store_dwordx2 v[64:65], v[48:49], off offset:2064
	v_mov_b64_e32 v[48:49], v[152:153]
	v_mov_b64_e32 v[50:51], v[154:155]
	v_pk_mul_f32 v[48:49], v[48:49], v[52:53]
	v_pk_mul_f32 v[52:53], v[58:59], v[66:67] op_sel_hi:[1,0]
	v_cvt_pk_bf16_f32 v48, v48, v49
	v_pk_mul_f32 v[50:51], v[50:51], v[52:53]
	v_pk_mul_f32 v[52:53], v[60:61], v[66:67] op_sel_hi:[1,0]
	v_cvt_pk_bf16_f32 v49, v50, v51
	global_store_dwordx2 v[64:65], v[48:49], off offset:2080
	v_mov_b64_e32 v[48:49], v[156:157]
	v_mov_b64_e32 v[50:51], v[158:159]
	v_pk_mul_f32 v[48:49], v[48:49], v[52:53]
	v_pk_mul_f32 v[52:53], v[62:63], v[66:67] op_sel_hi:[1,0]
	v_cvt_pk_bf16_f32 v48, v48, v49
	v_pk_mul_f32 v[50:51], v[50:51], v[52:53]
	s_nop 0
	v_cvt_pk_bf16_f32 v49, v50, v51
	global_store_dwordx2 v[64:65], v[48:49], off offset:2096
	v_mov_b64_e32 v[48:49], v[160:161]
	v_mov_b64_e32 v[50:51], v[162:163]
	v_pk_mul_f32 v[32:33], v[48:49], v[32:33]
	v_pk_mul_f32 v[34:35], v[50:51], v[34:35]
	v_cvt_pk_bf16_f32 v32, v32, v33
	v_cvt_pk_bf16_f32 v33, v34, v35
	global_store_dwordx2 v[64:65], v[32:33], off offset:2112
	v_mov_b64_e32 v[32:33], v[164:165]
	v_mov_b64_e32 v[34:35], v[166:167]
	v_pk_mul_f32 v[32:33], v[36:37], v[32:33]
	v_pk_mul_f32 v[36:37], v[38:39], v[66:67] op_sel_hi:[1,0]
	v_cvt_pk_bf16_f32 v32, v32, v33
	v_pk_mul_f32 v[34:35], v[36:37], v[34:35]
	v_pk_mul_f32 v[36:37], v[40:41], v[66:67] op_sel_hi:[1,0]
	v_cvt_pk_bf16_f32 v33, v34, v35
	global_store_dwordx2 v[64:65], v[32:33], off offset:2128
	v_mov_b64_e32 v[32:33], v[168:169]
	v_mov_b64_e32 v[34:35], v[170:171]
	v_pk_mul_f32 v[32:33], v[36:37], v[32:33]
	v_pk_mul_f32 v[36:37], v[42:43], v[66:67] op_sel_hi:[1,0]
	v_cvt_pk_bf16_f32 v32, v32, v33
	v_pk_mul_f32 v[34:35], v[36:37], v[34:35]
	v_pk_mul_f32 v[36:37], v[44:45], v[66:67] op_sel_hi:[1,0]
	v_cvt_pk_bf16_f32 v33, v34, v35
	global_store_dwordx2 v[64:65], v[32:33], off offset:2144
	v_mov_b64_e32 v[32:33], v[172:173]
	v_mov_b64_e32 v[34:35], v[174:175]
	v_pk_mul_f32 v[32:33], v[36:37], v[32:33]
	v_pk_mul_f32 v[36:37], v[46:47], v[66:67] op_sel_hi:[1,0]
	v_cvt_pk_bf16_f32 v32, v32, v33
	v_pk_mul_f32 v[34:35], v[36:37], v[34:35]
	s_nop 0
	v_cvt_pk_bf16_f32 v33, v34, v35
	global_store_dwordx2 v[64:65], v[32:33], off offset:2160
	v_mov_b64_e32 v[32:33], v[176:177]
	v_mov_b64_e32 v[34:35], v[178:179]
	v_pk_mul_f32 v[16:17], v[16:17], v[32:33]
	v_pk_mul_f32 v[18:19], v[18:19], v[34:35]
	v_cvt_pk_bf16_f32 v16, v16, v17
	v_cvt_pk_bf16_f32 v17, v18, v19
	global_store_dwordx2 v[64:65], v[16:17], off offset:2176
	v_mov_b64_e32 v[16:17], v[180:181]
	v_mov_b64_e32 v[18:19], v[182:183]
	v_pk_mul_f32 v[16:17], v[20:21], v[16:17]
	v_pk_mul_f32 v[20:21], v[22:23], v[66:67] op_sel_hi:[1,0]
	v_cvt_pk_bf16_f32 v16, v16, v17
	v_pk_mul_f32 v[18:19], v[20:21], v[18:19]
	v_pk_mul_f32 v[20:21], v[24:25], v[66:67] op_sel_hi:[1,0]
	v_cvt_pk_bf16_f32 v17, v18, v19
	global_store_dwordx2 v[64:65], v[16:17], off offset:2192
	v_mov_b64_e32 v[16:17], v[184:185]
	v_mov_b64_e32 v[18:19], v[186:187]
	v_pk_mul_f32 v[16:17], v[20:21], v[16:17]
	v_pk_mul_f32 v[20:21], v[26:27], v[66:67] op_sel_hi:[1,0]
	v_cvt_pk_bf16_f32 v16, v16, v17
	v_pk_mul_f32 v[18:19], v[20:21], v[18:19]
	v_pk_mul_f32 v[20:21], v[28:29], v[66:67] op_sel_hi:[1,0]
	v_cvt_pk_bf16_f32 v17, v18, v19
	global_store_dwordx2 v[64:65], v[16:17], off offset:2208
	v_mov_b64_e32 v[16:17], v[188:189]
	v_mov_b64_e32 v[18:19], v[190:191]
	v_pk_mul_f32 v[16:17], v[20:21], v[16:17]
	v_pk_mul_f32 v[20:21], v[30:31], v[66:67] op_sel_hi:[1,0]
	v_cvt_pk_bf16_f32 v16, v16, v17
	v_pk_mul_f32 v[18:19], v[20:21], v[18:19]
	s_nop 0
	v_cvt_pk_bf16_f32 v17, v18, v19
	global_store_dwordx2 v[64:65], v[16:17], off offset:2224
	v_mov_b64_e32 v[16:17], v[196:197]
	v_mov_b64_e32 v[18:19], v[198:199]
	v_pk_mul_f32 v[0:1], v[0:1], v[16:17]
	v_pk_mul_f32 v[2:3], v[2:3], v[18:19]
	v_cvt_pk_bf16_f32 v0, v0, v1
	v_cvt_pk_bf16_f32 v1, v2, v3
	global_store_dwordx2 v[64:65], v[0:1], off offset:2240
	v_mov_b64_e32 v[0:1], v[200:201]
	v_mov_b64_e32 v[2:3], v[202:203]
	v_pk_mul_f32 v[0:1], v[4:5], v[0:1]
	v_pk_mul_f32 v[4:5], v[6:7], v[66:67] op_sel_hi:[1,0]
	v_cvt_pk_bf16_f32 v0, v0, v1
	v_pk_mul_f32 v[2:3], v[4:5], v[2:3]
	v_pk_mul_f32 v[4:5], v[8:9], v[66:67] op_sel_hi:[1,0]
	v_cvt_pk_bf16_f32 v1, v2, v3
	global_store_dwordx2 v[64:65], v[0:1], off offset:2256
	v_mov_b64_e32 v[0:1], v[204:205]
	v_mov_b64_e32 v[2:3], v[206:207]
	v_pk_mul_f32 v[0:1], v[4:5], v[0:1]
	v_pk_mul_f32 v[4:5], v[10:11], v[66:67] op_sel_hi:[1,0]
	v_cvt_pk_bf16_f32 v0, v0, v1
	v_pk_mul_f32 v[2:3], v[4:5], v[2:3]
	v_pk_mul_f32 v[4:5], v[12:13], v[66:67] op_sel_hi:[1,0]
	v_cvt_pk_bf16_f32 v1, v2, v3
	global_store_dwordx2 v[64:65], v[0:1], off offset:2272
	v_mov_b64_e32 v[0:1], v[212:213]
	v_mov_b64_e32 v[2:3], v[214:215]
	v_pk_mul_f32 v[0:1], v[4:5], v[0:1]
	v_pk_mul_f32 v[4:5], v[14:15], v[66:67] op_sel_hi:[1,0]
	v_cvt_pk_bf16_f32 v0, v0, v1
	v_pk_mul_f32 v[2:3], v[4:5], v[2:3]
	s_nop 0
	v_cvt_pk_bf16_f32 v1, v2, v3
	global_store_dwordx2 v[64:65], v[0:1], off offset:2288
	s_barrier
	s_cbranch_scc0 .LBB0_443

; __device__ __forceinline__ void attn_unit(const Frame& F, const bf16* __restrict__ proj, bf16* mix, const float* relb, const float* subg, int h, int qb, float lam, float one_m_li) {
;     ...
;     if (m == 0) {
;         float ss = 0.f;
; #pragma unroll
;         for (int eb = 0; eb < 4; ++eb)
; #pragma unroll
;             for (int r = 0; r < 16; ++r) { const float v = o[eb][r] - lam * xch[(wq * 64 + eb * 16 + r) * 64 + lane]; o[eb][r] = v; ss += v * v; }
.LBB0_594:
	s_andn2_b64 vcc, exec, s[44:45]
	s_waitcnt lgkmcnt(0)
	s_barrier
	s_cbranch_vccnz .LBB0_563
	v_lshl_add_u32 v126, v213, 2, s56
	ds_read2st64_b32 v[10:11], v126 offset1:1
	ds_read2st64_b32 v[12:13], v126 offset0:2 offset1:3
	ds_read2st64_b32 v[14:15], v126 offset0:4 offset1:5
	ds_read2st64_b32 v[28:29], v126 offset0:6 offset1:7
	ds_read2st64_b32 v[46:47], v126 offset0:8 offset1:9
	ds_read2st64_b32 v[62:63], v126 offset0:10 offset1:11
	ds_read2st64_b32 v[76:77], v126 offset0:12 offset1:13
	ds_read2st64_b32 v[78:79], v126 offset0:14 offset1:15
	ds_read2st64_b32 v[80:81], v126 offset0:16 offset1:17
	ds_read2st64_b32 v[82:83], v126 offset0:18 offset1:19
	ds_read2st64_b32 v[84:85], v126 offset0:20 offset1:21
	ds_read2st64_b32 v[86:87], v126 offset0:22 offset1:23
	ds_read2st64_b32 v[88:89], v126 offset0:24 offset1:25
	ds_read2st64_b32 v[90:91], v126 offset0:26 offset1:27
	ds_read2st64_b32 v[92:93], v126 offset0:28 offset1:29
	ds_read2st64_b32 v[94:95], v126 offset0:30 offset1:31
	ds_read2st64_b32 v[96:97], v126 offset0:32 offset1:33
	ds_read2st64_b32 v[98:99], v126 offset0:34 offset1:35
	ds_read2st64_b32 v[100:101], v126 offset0:36 offset1:37
	ds_read2st64_b32 v[102:103], v126 offset0:38 offset1:39
	ds_read2st64_b32 v[104:105], v126 offset0:40 offset1:41
	ds_read2st64_b32 v[106:107], v126 offset0:42 offset1:43
	ds_read2st64_b32 v[108:109], v126 offset0:44 offset1:45
	ds_read2st64_b32 v[110:111], v126 offset0:46 offset1:47
	ds_read2st64_b32 v[112:113], v126 offset0:56 offset1:57
	ds_read2st64_b32 v[114:115], v126 offset0:58 offset1:59
	ds_read2st64_b32 v[116:117], v126 offset0:60 offset1:61
	ds_read2st64_b32 v[118:119], v126 offset0:62 offset1:63
	ds_read2st64_b32 v[120:121], v126 offset0:48 offset1:49
	ds_read2st64_b32 v[122:123], v126 offset0:50 offset1:51
	ds_read2st64_b32 v[124:125], v126 offset0:52 offset1:53
	ds_read2st64_b32 v[126:127], v126 offset0:54 offset1:55
	s_waitcnt lgkmcnt(14)
	v_pk_fma_f32 v[70:71], v[160:161], v[10:11], v[70:71] neg_lo:[1,0,0] neg_hi:[1,0,0]
	v_pk_fma_f32 v[74:75], v[160:161], v[12:13], v[74:75] neg_lo:[1,0,0] neg_hi:[1,0,0]
	s_waitcnt vmcnt(3)
	v_pk_mul_f32 v[130:131], v[70:71], v[70:71]
	v_pk_mul_f32 v[128:129], v[74:75], v[74:75]
	s_waitcnt lgkmcnt(1)
	v_pk_fma_f32 v[12:13], v[160:161], v[124:125], v[4:5] neg_lo:[1,0,0] neg_hi:[1,0,0]
	v_pk_fma_f32 v[4:5], v[160:161], v[114:115], v[8:9] neg_lo:[1,0,0] neg_hi:[1,0,0]
	v_pk_fma_f32 v[8:9], v[160:161], v[112:113], v[2:3] neg_lo:[1,0,0] neg_hi:[1,0,0]
	v_pk_fma_f32 v[2:3], v[160:161], v[116:117], v[16:17] neg_lo:[1,0,0] neg_hi:[1,0,0]
	v_add_f32_e32 v116, v130, v131
	v_pk_fma_f32 v[66:67], v[160:161], v[14:15], v[66:67] neg_lo:[1,0,0] neg_hi:[1,0,0]
	v_add_f32_e32 v116, v116, v128
	s_waitcnt vmcnt(2)
	v_pk_mul_f32 v[134:135], v[66:67], v[66:67]
	v_add_f32_e32 v116, v116, v129
	v_pk_fma_f32 v[72:73], v[160:161], v[28:29], v[72:73] neg_lo:[1,0,0] neg_hi:[1,0,0]
	v_add_f32_e32 v116, v116, v134
	v_pk_mul_f32 v[132:133], v[72:73], v[72:73]
	v_add_f32_e32 v116, v116, v135
	v_pk_fma_f32 v[64:65], v[160:161], v[46:47], v[64:65] neg_lo:[1,0,0] neg_hi:[1,0,0]
	v_add_f32_e32 v116, v116, v132
	s_waitcnt vmcnt(1)
	v_pk_mul_f32 v[136:137], v[64:65], v[64:65]
	v_add_f32_e32 v116, v116, v133
	v_pk_fma_f32 v[62:63], v[160:161], v[62:63], v[68:69] neg_lo:[1,0,0] neg_hi:[1,0,0]
	v_add_f32_e32 v116, v116, v136
	v_pk_mul_f32 v[68:69], v[62:63], v[62:63]
	v_add_f32_e32 v116, v116, v137
	v_pk_fma_f32 v[54:55], v[160:161], v[76:77], v[54:55] neg_lo:[1,0,0] neg_hi:[1,0,0]
	v_add_f32_e32 v68, v116, v68
	v_pk_mul_f32 v[76:77], v[54:55], v[54:55]
	v_add_f32_e32 v68, v68, v69
	v_pk_fma_f32 v[60:61], v[160:161], v[78:79], v[60:61] neg_lo:[1,0,0] neg_hi:[1,0,0]
	v_add_f32_e32 v68, v68, v76
	v_pk_mul_f32 v[78:79], v[60:61], v[60:61]
	v_add_f32_e32 v68, v68, v77
	v_pk_fma_f32 v[80:81], v[160:161], v[80:81], v[50:51] neg_lo:[1,0,0] neg_hi:[1,0,0]
	v_add_f32_e32 v68, v68, v78
	v_pk_mul_f32 v[50:51], v[80:81], v[80:81]
	v_add_f32_e32 v68, v68, v79
	v_pk_fma_f32 v[58:59], v[160:161], v[82:83], v[58:59] neg_lo:[1,0,0] neg_hi:[1,0,0]
	v_add_f32_e32 v50, v68, v50
	v_pk_mul_f32 v[82:83], v[58:59], v[58:59]
	v_add_f32_e32 v50, v50, v51
	v_pk_fma_f32 v[84:85], v[160:161], v[84:85], v[48:49] neg_lo:[1,0,0] neg_hi:[1,0,0]
	v_add_f32_e32 v50, v50, v82
	v_pk_mul_f32 v[48:49], v[84:85], v[84:85]
	v_add_f32_e32 v50, v50, v83
	v_pk_fma_f32 v[56:57], v[160:161], v[86:87], v[56:57] neg_lo:[1,0,0] neg_hi:[1,0,0]
	v_add_f32_e32 v48, v50, v48
	v_pk_mul_f32 v[86:87], v[56:57], v[56:57]
	v_add_f32_e32 v48, v48, v49
	v_pk_fma_f32 v[88:89], v[160:161], v[88:89], v[40:41] neg_lo:[1,0,0] neg_hi:[1,0,0]
	v_add_f32_e32 v48, v48, v86
	v_pk_fma_f32 v[46:47], v[160:161], v[90:91], v[52:53] neg_lo:[1,0,0] neg_hi:[1,0,0]
	v_pk_mul_f32 v[90:91], v[88:89], v[88:89]
	v_add_f32_e32 v48, v48, v87
	v_add_f32_e32 v48, v48, v90
	v_pk_mul_f32 v[52:53], v[46:47], v[46:47]
	v_add_f32_e32 v48, v48, v91
	v_pk_fma_f32 v[40:41], v[160:161], v[94:95], v[44:45] neg_lo:[1,0,0] neg_hi:[1,0,0]
	v_pk_fma_f32 v[44:45], v[160:161], v[92:93], v[36:37] neg_lo:[1,0,0] neg_hi:[1,0,0]
	v_add_f32_e32 v48, v48, v52
	v_pk_mul_f32 v[92:93], v[44:45], v[44:45]
	v_add_f32_e32 v48, v48, v53
	v_add_f32_e32 v48, v48, v92
	v_pk_mul_f32 v[94:95], v[40:41], v[40:41]
	v_add_f32_e32 v48, v48, v93
	v_pk_fma_f32 v[34:35], v[160:161], v[96:97], v[34:35] neg_lo:[1,0,0] neg_hi:[1,0,0]
	v_add_f32_e32 v48, v48, v94
	v_pk_mul_f32 v[96:97], v[34:35], v[34:35]
	v_add_f32_e32 v48, v48, v95
	v_pk_fma_f32 v[36:37], v[160:161], v[98:99], v[42:43] neg_lo:[1,0,0] neg_hi:[1,0,0]
	v_add_f32_e32 v48, v48, v96
	v_pk_mul_f32 v[42:43], v[36:37], v[36:37]
	v_add_f32_e32 v48, v48, v97
; __device__ __forceinline__ float swap_sum(float v) { float r0, r1; swap32(v, r0, r1); return r0 + r1; }
; __device__ __forceinline__ unsigned cvt_pk_bf16(float lo, float hi) { typedef __bf16 bf16x2_t __attribute__((ext_vector_type(2))); f32x2 v = {lo, hi}; bf16x2_t b = __builtin_convertvector(v, bf16x2_t); return __builtin_bit_cast(unsigned, b); }
; __device__ __forceinline__ void attn_unit(const Frame& F, const bf16* __restrict__ proj, bf16* mix, const float* relb, const float* subg, int h, int qb, float lam, float one_m_li) {
;     ...
;         ss = swap_sum(ss);
;         const float rstd = rsqrtf(ss * (1.0f / 128.0f) + EPS) * one_m_li;
;         bf16* orow = mix + (size_t)qrow * D + 1536 + h * 128;
; #pragma unroll
;         for (int eb = 0; eb < 4; ++eb)
; #pragma unroll
;             for (int rq = 0; rq < 4; ++rq) { const int e0 = 32 * eb + 8 * rq + 4 * hi;
;                 const f32x4 gq = *(const f32x4*)(subg + e0);
;                 u32x2 wv; wv.x = gm::cvt_pk_bf16(o[eb][4 * rq + 0] * rstd * gq.x, o[eb][4 * rq + 1] * rstd * gq.y); wv.y = gm::cvt_pk_bf16(o[eb][4 * rq + 2] * rstd * gq.z, o[eb][4 * rq + 3] * rstd * gq.w);
;                 *(u32x2*)(orow + e0) = wv; }
	v_pk_fma_f32 v[32:33], v[160:161], v[100:101], v[32:33] neg_lo:[1,0,0] neg_hi:[1,0,0]
	v_add_f32_e32 v42, v48, v42
	v_pk_mul_f32 v[98:99], v[32:33], v[32:33]
	v_add_f32_e32 v42, v42, v43
	v_pk_fma_f32 v[28:29], v[160:161], v[102:103], v[38:39] neg_lo:[1,0,0] neg_hi:[1,0,0]
	v_add_f32_e32 v42, v42, v98
	v_pk_mul_f32 v[38:39], v[28:29], v[28:29]
	v_add_f32_e32 v42, v42, v99
	v_pk_fma_f32 v[24:25], v[160:161], v[104:105], v[24:25] neg_lo:[1,0,0] neg_hi:[1,0,0]
	v_add_f32_e32 v38, v42, v38
	v_pk_mul_f32 v[102:103], v[24:25], v[24:25]
	v_add_f32_e32 v38, v38, v39
	v_pk_fma_f32 v[22:23], v[160:161], v[106:107], v[22:23] neg_lo:[1,0,0] neg_hi:[1,0,0]
	v_add_f32_e32 v38, v38, v102
	v_pk_mul_f32 v[100:101], v[22:23], v[22:23]
	v_add_f32_e32 v38, v38, v103
	v_pk_fma_f32 v[20:21], v[160:161], v[108:109], v[20:21] neg_lo:[1,0,0] neg_hi:[1,0,0]
	v_add_f32_e32 v38, v38, v100
	v_pk_mul_f32 v[104:105], v[20:21], v[20:21]
	v_add_f32_e32 v38, v38, v101
	v_pk_fma_f32 v[14:15], v[160:161], v[110:111], v[30:31] neg_lo:[1,0,0] neg_hi:[1,0,0]
	v_add_f32_e32 v38, v38, v104
	v_pk_mul_f32 v[30:31], v[14:15], v[14:15]
	v_add_f32_e32 v38, v38, v105
	v_pk_fma_f32 v[18:19], v[160:161], v[120:121], v[18:19] neg_lo:[1,0,0] neg_hi:[1,0,0]
	v_add_f32_e32 v30, v38, v30
	v_pk_mul_f32 v[106:107], v[18:19], v[18:19]
	v_add_f32_e32 v30, v30, v31
	v_pk_fma_f32 v[10:11], v[160:161], v[122:123], v[26:27] neg_lo:[1,0,0] neg_hi:[1,0,0]
	v_add_f32_e32 v30, v30, v106
	v_pk_mul_f32 v[26:27], v[10:11], v[10:11]
	v_add_f32_e32 v30, v30, v107
	v_add_f32_e32 v26, v30, v26
	v_pk_mul_f32 v[110:111], v[12:13], v[12:13]
	v_add_f32_e32 v26, v26, v27
	s_waitcnt lgkmcnt(0)
	v_pk_fma_f32 v[6:7], v[160:161], v[126:127], v[6:7] neg_lo:[1,0,0] neg_hi:[1,0,0]
	v_add_f32_e32 v26, v26, v110
	v_pk_mul_f32 v[108:109], v[6:7], v[6:7]
	v_add_f32_e32 v26, v26, v111
	v_add_f32_e32 v26, v26, v108
	v_pk_mul_f32 v[112:113], v[8:9], v[8:9]
	v_add_f32_e32 v26, v26, v109
	v_add_f32_e32 v26, v26, v112
	v_pk_mul_f32 v[114:115], v[4:5], v[4:5]
	v_add_f32_e32 v26, v26, v113
	v_add_f32_e32 v26, v26, v114
	v_pk_mul_f32 v[16:17], v[2:3], v[2:3]
	v_add_f32_e32 v26, v26, v115
	v_pk_fma_f32 v[0:1], v[160:161], v[118:119], v[0:1] neg_lo:[1,0,0] neg_hi:[1,0,0]
	v_add_f32_e32 v16, v26, v16
	v_pk_mul_f32 v[118:119], v[0:1], v[0:1]
	v_add_f32_e32 v16, v16, v17
	v_add_f32_e32 v16, v16, v118
	v_add_f32_e32 v26, v16, v119
	v_mov_b32_e32 v27, v26
	s_nop 1
	v_permlane32_swap_b32 v27, v26
	global_load_dwordx4 v[144:147], v192, s[36:37]
	global_load_dwordx4 v[148:151], v192, s[36:37] offset:32
	global_load_dwordx4 v[152:155], v192, s[36:37] offset:64
	global_load_dwordx4 v[156:159], v192, s[36:37] offset:96
	global_load_dwordx4 v[168:171], v192, s[36:37] offset:128
	global_load_dwordx4 v[172:175], v192, s[36:37] offset:160
	global_load_dwordx4 v[176:179], v192, s[36:37] offset:192
	global_load_dwordx4 v[180:183], v192, s[36:37] offset:224
	global_load_dwordx4 v[196:199], v192, s[36:37] offset:256
	global_load_dwordx4 v[200:203], v192, s[36:37] offset:288
	global_load_dwordx4 v[224:227], v192, s[36:37] offset:320
	global_load_dwordx4 v[228:231], v192, s[36:37] offset:352
	global_load_dwordx4 v[232:235], v192, s[36:37] offset:384
	global_load_dwordx4 v[236:239], v192, s[36:37] offset:416
	global_load_dwordx4 v[240:243], v192, s[36:37] offset:448
	global_load_dwordx4 v[244:247], v192, s[36:37] offset:480
	v_add_f32_e32 v26, v27, v26
	v_fmamk_f32 v26, v26, 0x3c000000, v194
	v_mul_f32_e32 v27, 0x4b800000, v26
	v_cmp_gt_f32_e32 vcc, s26, v26
	v_lshlrev_b32_e32 v16, 12, v188
	v_mov_b32_e32 v17, v193
	v_cndmask_b32_e32 v26, v26, v27, vcc
	v_rsq_f32_e32 v30, v26
	v_lshl_add_u64 v[16:17], s[42:43], 0, v[16:17]
	v_lshl_add_u64 v[16:17], s[48:49], 1, v[16:17]
	v_lshlrev_b32_e32 v26, 3, v187
	v_mov_b32_e32 v27, v193
	v_lshl_add_u64 v[16:17], v[16:17], 0, v[26:27]
	v_mul_f32_e32 v26, 0x45800000, v30
	v_cndmask_b32_e32 v26, v30, v26, vcc
	v_mul_f32_e32 v30, v186, v26
	v_pk_mul_f32 v[26:27], v[70:71], v[30:31] op_sel_hi:[1,0]
	v_pk_mul_f32 v[38:39], v[74:75], v[30:31] op_sel_hi:[1,0]
	s_mov_b32 s8, 0x42100000
	v_pk_mul_f32 v[22:23], v[22:23], v[30:31] op_sel_hi:[1,0]
	v_pk_mul_f32 v[14:15], v[14:15], v[30:31] op_sel_hi:[1,0]
	v_pk_mul_f32 v[18:19], v[18:19], v[30:31] op_sel_hi:[1,0]
	v_pk_mul_f32 v[10:11], v[10:11], v[30:31] op_sel_hi:[1,0]
	v_pk_mul_f32 v[6:7], v[6:7], v[30:31] op_sel_hi:[1,0]
	v_pk_mul_f32 v[4:5], v[4:5], v[30:31] op_sel_hi:[1,0]
	v_pk_mul_f32 v[2:3], v[2:3], v[30:31] op_sel_hi:[1,0]
	v_pk_mul_f32 v[0:1], v[0:1], v[30:31] op_sel_hi:[1,0]
	s_waitcnt vmcnt(15)
	v_mov_b64_e32 v[48:49], v[144:145]
	v_mov_b64_e32 v[50:51], v[146:147]
	v_pk_mul_f32 v[26:27], v[48:49], v[26:27]
	v_pk_mul_f32 v[38:39], v[50:51], v[38:39]
	v_cvt_pk_bf16_f32 v26, v26, v27
	v_cvt_pk_bf16_f32 v27, v38, v39
	v_add_co_u32_e32 v38, vcc, s8, v16
	s_mov_b64 s[8:9], 0x42100c00
	s_nop 0
	v_addc_co_u32_e32 v39, vcc, 0, v17, vcc
	global_store_dwordx2 v[38:39], v[26:27], off offset:3072
	v_lshl_add_u64 v[42:43], v[16:17], 0, s[8:9]
	v_pk_mul_f32 v[16:17], v[66:67], v[30:31] op_sel_hi:[1,0]
	v_pk_mul_f32 v[26:27], v[72:73], v[30:31] op_sel_hi:[1,0]
	s_waitcnt vmcnt(15)
	v_mov_b64_e32 v[48:49], v[148:149]
	v_mov_b64_e32 v[50:51], v[150:151]
	v_pk_mul_f32 v[16:17], v[48:49], v[16:17]
	v_pk_mul_f32 v[26:27], v[50:51], v[26:27]
	v_cvt_pk_bf16_f32 v16, v16, v17
	v_cvt_pk_bf16_f32 v17, v26, v27
	global_store_dwordx2 v[42:43], v[16:17], off offset:16
	v_pk_mul_f32 v[16:17], v[64:65], v[30:31] op_sel_hi:[1,0]
	v_pk_mul_f32 v[26:27], v[62:63], v[30:31] op_sel_hi:[1,0]
	s_waitcnt vmcnt(15)
; __device__ __forceinline__ unsigned cvt_pk_bf16(float lo, float hi) { typedef __bf16 bf16x2_t __attribute__((ext_vector_type(2))); f32x2 v = {lo, hi}; bf16x2_t b = __builtin_convertvector(v, bf16x2_t); return __builtin_bit_cast(unsigned, b); }
; __device__ __forceinline__ void attn_unit(const Frame& F, const bf16* __restrict__ proj, bf16* mix, const float* relb, const float* subg, int h, int qb, float lam, float one_m_li) {
;     ...
; #pragma unroll
;         for (int eb = 0; eb < 4; ++eb)
; #pragma unroll
;             for (int rq = 0; rq < 4; ++rq) { const int e0 = 32 * eb + 8 * rq + 4 * hi;
;                 const f32x4 gq = *(const f32x4*)(subg + e0);
;                 u32x2 wv; wv.x = gm::cvt_pk_bf16(o[eb][4 * rq + 0] * rstd * gq.x, o[eb][4 * rq + 1] * rstd * gq.y); wv.y = gm::cvt_pk_bf16(o[eb][4 * rq + 2] * rstd * gq.z, o[eb][4 * rq + 3] * rstd * gq.w);
;                 *(u32x2*)(orow + e0) = wv; }
	v_mov_b64_e32 v[48:49], v[152:153]
	v_mov_b64_e32 v[50:51], v[154:155]
	v_pk_mul_f32 v[16:17], v[48:49], v[16:17]
	v_pk_mul_f32 v[26:27], v[50:51], v[26:27]
	v_cvt_pk_bf16_f32 v16, v16, v17
	v_cvt_pk_bf16_f32 v17, v26, v27
	global_store_dwordx2 v[42:43], v[16:17], off offset:32
	v_pk_mul_f32 v[16:17], v[54:55], v[30:31] op_sel_hi:[1,0]
	v_pk_mul_f32 v[26:27], v[60:61], v[30:31] op_sel_hi:[1,0]
	s_waitcnt vmcnt(15)
	v_mov_b64_e32 v[48:49], v[156:157]
	v_mov_b64_e32 v[50:51], v[158:159]
	v_pk_mul_f32 v[16:17], v[48:49], v[16:17]
	v_pk_mul_f32 v[26:27], v[50:51], v[26:27]
	v_cvt_pk_bf16_f32 v16, v16, v17
	v_cvt_pk_bf16_f32 v17, v26, v27
	global_store_dwordx2 v[42:43], v[16:17], off offset:48
	v_pk_mul_f32 v[16:17], v[80:81], v[30:31] op_sel_hi:[1,0]
	v_pk_mul_f32 v[26:27], v[58:59], v[30:31] op_sel_hi:[1,0]
	s_waitcnt vmcnt(15)
	v_mov_b64_e32 v[48:49], v[168:169]
	v_mov_b64_e32 v[50:51], v[170:171]
	v_pk_mul_f32 v[16:17], v[48:49], v[16:17]
	v_pk_mul_f32 v[26:27], v[50:51], v[26:27]
	v_cvt_pk_bf16_f32 v16, v16, v17
	v_cvt_pk_bf16_f32 v17, v26, v27
	global_store_dwordx2 v[42:43], v[16:17], off offset:64
	v_pk_mul_f32 v[16:17], v[84:85], v[30:31] op_sel_hi:[1,0]
	v_pk_mul_f32 v[26:27], v[56:57], v[30:31] op_sel_hi:[1,0]
	s_waitcnt vmcnt(15)
	v_mov_b64_e32 v[48:49], v[172:173]
	v_mov_b64_e32 v[50:51], v[174:175]
	v_pk_mul_f32 v[16:17], v[16:17], v[48:49]
	v_pk_mul_f32 v[26:27], v[26:27], v[50:51]
	v_cvt_pk_bf16_f32 v16, v16, v17
	v_cvt_pk_bf16_f32 v17, v26, v27
	global_store_dwordx2 v[42:43], v[16:17], off offset:80
	v_pk_mul_f32 v[16:17], v[88:89], v[30:31] op_sel_hi:[1,0]
	v_pk_mul_f32 v[26:27], v[46:47], v[30:31] op_sel_hi:[1,0]
	s_waitcnt vmcnt(15)
	v_mov_b64_e32 v[48:49], v[176:177]
	v_mov_b64_e32 v[50:51], v[178:179]
	v_pk_mul_f32 v[16:17], v[16:17], v[48:49]
	v_pk_mul_f32 v[26:27], v[26:27], v[50:51]
	v_cvt_pk_bf16_f32 v16, v16, v17
	v_cvt_pk_bf16_f32 v17, v26, v27
	global_store_dwordx2 v[42:43], v[16:17], off offset:96
	v_pk_mul_f32 v[16:17], v[44:45], v[30:31] op_sel_hi:[1,0]
	v_pk_mul_f32 v[26:27], v[40:41], v[30:31] op_sel_hi:[1,0]
	s_waitcnt vmcnt(15)
	v_mov_b64_e32 v[46:47], v[180:181]
	v_mov_b64_e32 v[48:49], v[182:183]
	v_pk_mul_f32 v[16:17], v[16:17], v[46:47]
	v_pk_mul_f32 v[26:27], v[26:27], v[48:49]
	v_cvt_pk_bf16_f32 v16, v16, v17
	v_cvt_pk_bf16_f32 v17, v26, v27
	global_store_dwordx2 v[42:43], v[16:17], off offset:112
	v_pk_mul_f32 v[16:17], v[34:35], v[30:31] op_sel_hi:[1,0]
	v_pk_mul_f32 v[26:27], v[36:37], v[30:31] op_sel_hi:[1,0]
	s_waitcnt vmcnt(15)
	v_mov_b64_e32 v[38:39], v[196:197]
	v_mov_b64_e32 v[40:41], v[198:199]
	v_pk_mul_f32 v[16:17], v[16:17], v[38:39]
	v_pk_mul_f32 v[26:27], v[26:27], v[40:41]
	v_cvt_pk_bf16_f32 v16, v16, v17
	v_cvt_pk_bf16_f32 v17, v26, v27
	global_store_dwordx2 v[42:43], v[16:17], off offset:128
	v_pk_mul_f32 v[16:17], v[32:33], v[30:31] op_sel_hi:[1,0]
	v_pk_mul_f32 v[26:27], v[28:29], v[30:31] op_sel_hi:[1,0]
	s_waitcnt vmcnt(15)
	v_mov_b64_e32 v[34:35], v[200:201]
	v_mov_b64_e32 v[36:37], v[202:203]
	v_pk_mul_f32 v[16:17], v[16:17], v[34:35]
	v_pk_mul_f32 v[26:27], v[26:27], v[36:37]
	v_cvt_pk_bf16_f32 v16, v16, v17
	v_cvt_pk_bf16_f32 v17, v26, v27
	global_store_dwordx2 v[42:43], v[16:17], off offset:144
	v_pk_mul_f32 v[16:17], v[24:25], v[30:31] op_sel_hi:[1,0]
	s_waitcnt vmcnt(15)
	v_mov_b64_e32 v[26:27], v[224:225]
	v_mov_b64_e32 v[28:29], v[226:227]
	v_pk_mul_f32 v[22:23], v[22:23], v[28:29]
	v_pk_mul_f32 v[16:17], v[16:17], v[26:27]
	s_nop 0
	v_cvt_pk_bf16_f32 v16, v16, v17
	v_cvt_pk_bf16_f32 v17, v22, v23
	global_store_dwordx2 v[42:43], v[16:17], off offset:160
	v_pk_mul_f32 v[16:17], v[20:21], v[30:31] op_sel_hi:[1,0]
	s_waitcnt vmcnt(15)
	v_mov_b64_e32 v[22:23], v[228:229]
	v_mov_b64_e32 v[24:25], v[230:231]
	v_pk_mul_f32 v[14:15], v[14:15], v[24:25]
	v_pk_mul_f32 v[16:17], v[16:17], v[22:23]
	s_nop 0
	v_cvt_pk_bf16_f32 v16, v16, v17
	v_cvt_pk_bf16_f32 v17, v14, v15
	global_store_dwordx2 v[42:43], v[16:17], off offset:176
	s_waitcnt vmcnt(15)
	v_mov_b64_e32 v[14:15], v[232:233]
	v_mov_b64_e32 v[16:17], v[234:235]
	v_pk_mul_f32 v[14:15], v[18:19], v[14:15]
	v_pk_mul_f32 v[10:11], v[10:11], v[16:17]
	v_cvt_pk_bf16_f32 v14, v14, v15
	v_cvt_pk_bf16_f32 v15, v10, v11
	global_store_dwordx2 v[42:43], v[14:15], off offset:192
	v_pk_mul_f32 v[10:11], v[12:13], v[30:31] op_sel_hi:[1,0]
	s_waitcnt vmcnt(15)
	v_mov_b64_e32 v[14:15], v[236:237]
	v_mov_b64_e32 v[16:17], v[238:239]
	v_pk_mul_f32 v[6:7], v[6:7], v[16:17]
	v_pk_mul_f32 v[10:11], v[10:11], v[14:15]
	s_nop 0
	v_cvt_pk_bf16_f32 v10, v10, v11
	v_cvt_pk_bf16_f32 v11, v6, v7
	global_store_dwordx2 v[42:43], v[10:11], off offset:208
	v_pk_mul_f32 v[6:7], v[8:9], v[30:31] op_sel_hi:[1,0]
	s_waitcnt vmcnt(15)
	v_mov_b64_e32 v[10:11], v[240:241]
	v_mov_b64_e32 v[12:13], v[242:243]
	v_pk_mul_f32 v[4:5], v[4:5], v[12:13]
	v_pk_mul_f32 v[6:7], v[6:7], v[10:11]
	s_nop 0
	v_cvt_pk_bf16_f32 v6, v6, v7
	v_cvt_pk_bf16_f32 v7, v4, v5
	global_store_dwordx2 v[42:43], v[6:7], off offset:224
	s_waitcnt vmcnt(15)
	v_mov_b64_e32 v[4:5], v[244:245]
	v_mov_b64_e32 v[6:7], v[246:247]
	v_pk_mul_f32 v[2:3], v[2:3], v[4:5]
	v_pk_mul_f32 v[0:1], v[0:1], v[6:7]
	v_cvt_pk_bf16_f32 v2, v2, v3
	v_cvt_pk_bf16_f32 v3, v0, v1
	global_store_dwordx2 v[42:43], v[2:3], off offset:240
	s_branch .LBB0_563

; __device__ __forceinline__ unsigned cvt_pk_bf16(float lo, float hi) { typedef __bf16 bf16x2_t __attribute__((ext_vector_type(2))); f32x2 v = {lo, hi}; bf16x2_t b = __builtin_convertvector(v, bf16x2_t); return __builtin_bit_cast(unsigned, b); }
; __device__ __forceinline__ void s5_final_chunk(const Frame& F, const unsigned char* tab, const bf16* __restrict__ proj, f32x2* E, const bf16* __restrict__ wglu_t, const float* mixg, bf16* mix, int c) {
;     ...
;     for (int tt = 0; tt < 2; ++tt) { const int t = 32 * tt + r32; float tot = 0.f;
; #pragma unroll
;         for (int ww = 0; ww < 8; ++ww) tot += red[ww * 64 + t];
;         const float rstd = rsqrtf(tot * (1.0f / 512.0f) + EPS);
;         bf16* orow = mix + (size_t)(64 * c + t) * D;
; #pragma unroll
;         for (int nt = 0; nt < 2; ++nt)
; #pragma unroll
;             for (int rq = 0; rq < 4; ++rq) { const int n4 = n0 + 32 * nt + 8 * rq + 4 * hi; const f32x4 gq = *(const f32x4*)(mixg + n4);
;                 u32x2 wv; wv.x = gm::cvt_pk_bf16(z[nt][tt][4 * rq + 0] * rstd * gq.x, z[nt][tt][4 * rq + 1] * rstd * gq.y); wv.y = gm::cvt_pk_bf16(z[nt][tt][4 * rq + 2] * rstd * gq.z, z[nt][tt][4 * rq + 3] * rstd * gq.w);
;                 *(u32x2*)(orow + n4) = wv; } }
.LBB0_649:
	s_or_b64 exec, exec, s[8:9]
	v_lshl_add_u32 v66, v125, 2, s22
	v_ashrrev_i32_e32 v67, 31, v66
	v_lshl_add_u64 v[64:65], v[66:67], 2, s[80:81]
	s_waitcnt lgkmcnt(0)
	s_barrier
	global_load_dwordx4 v[196:199], v[64:65], off
	global_load_dwordx4 v[200:203], v[64:65], off offset:32
	global_load_dwordx4 v[204:207], v[64:65], off offset:64
	global_load_dwordx4 v[208:211], v[64:65], off offset:96
	global_load_dwordx4 v[212:215], v[64:65], off offset:128
	global_load_dwordx4 v[216:219], v[64:65], off offset:160
	global_load_dwordx4 v[220:223], v[64:65], off offset:192
	global_load_dwordx4 v[224:227], v[64:65], off offset:224
	s_add_i32 s8, 0, 0x21400
	v_lshl_add_u32 v90, v68, 2, s8
	v_lshl_add_u32 v69, v124, 2, s8
	ds_read2st64_b32 v[76:77], v90 offset1:1
	ds_read2st64_b32 v[78:79], v69 offset1:1
	ds_read2st64_b32 v[80:81], v69 offset0:2 offset1:3
	ds_read2st64_b32 v[82:83], v69 offset0:4 offset1:5
	ds_read2st64_b32 v[84:85], v69 offset0:6 offset1:7
	ds_read2st64_b32 v[86:87], v90 offset0:2 offset1:3
	ds_read2st64_b32 v[88:89], v90 offset0:4 offset1:5
	ds_read2st64_b32 v[90:91], v90 offset0:6 offset1:7
	s_waitcnt lgkmcnt(7)
	v_mov_b32_e32 v92, v76
	s_waitcnt lgkmcnt(6)
	v_mov_b32_e32 v93, v78
	v_mov_b32_e32 v78, v77
	s_waitcnt lgkmcnt(2)
	v_mov_b32_e32 v76, v86
	v_mov_b32_e32 v77, v80
	v_mov_b32_e32 v80, v87
	s_waitcnt lgkmcnt(1)
	v_mov_b32_e32 v86, v88
	v_mov_b32_e32 v87, v82
	v_mov_b32_e32 v82, v89
	s_waitcnt lgkmcnt(0)
	v_mov_b32_e32 v88, v90
	v_mov_b32_e32 v89, v84
	v_mov_b32_e32 v84, v91
	v_pk_add_f32 v[90:91], v[92:93], 0 op_sel_hi:[1,0]
	s_mov_b32 s8, 0x3b000000
	v_pk_add_f32 v[78:79], v[90:91], v[78:79]
	v_lshlrev_b64 v[74:75], 12, v[94:95]
	v_pk_add_f32 v[76:77], v[78:79], v[76:77]
	v_lshl_add_u64 v[74:75], s[46:47], 0, v[74:75]
	v_pk_add_f32 v[76:77], v[76:77], v[80:81]
	v_lshlrev_b64 v[66:67], 1, v[66:67]
	v_pk_add_f32 v[76:77], v[76:77], v[86:87]
	v_lshl_add_u64 v[74:75], v[74:75], 0, v[66:67]
	v_pk_add_f32 v[76:77], v[76:77], v[82:83]
	s_add_i32 s4, s4, s2
	v_pk_add_f32 v[76:77], v[76:77], v[88:89]
	s_cmpk_gt_i32 s4, 0xff
	v_pk_add_f32 v[76:77], v[76:77], v[84:85]
	s_nop 0
	v_pk_fma_f32 v[76:77], v[76:77], s[8:9], v[194:195] op_sel_hi:[1,0,0]
	s_nop 0
	v_mul_f32_e32 v69, 0x4b800000, v77
	v_cmp_gt_f32_e32 vcc, s26, v77
	s_nop 1
	v_cndmask_b32_e32 v69, v77, v69, vcc
	v_rsq_f32_e32 v69, v69
	s_nop 0
	v_mul_f32_e32 v77, 0x45800000, v69
	v_cndmask_b32_e32 v78, v69, v77, vcc
	v_pk_mul_f32 v[48:49], v[48:49], v[78:79] op_sel_hi:[1,0]
	v_pk_mul_f32 v[50:51], v[50:51], v[78:79] op_sel_hi:[1,0]
	v_pk_mul_f32 v[52:53], v[52:53], v[78:79] op_sel_hi:[1,0]
	v_pk_mul_f32 v[54:55], v[54:55], v[78:79] op_sel_hi:[1,0]
	v_pk_mul_f32 v[32:33], v[32:33], v[78:79] op_sel_hi:[1,0]
	v_pk_mul_f32 v[34:35], v[34:35], v[78:79] op_sel_hi:[1,0]
	v_pk_mul_f32 v[36:37], v[36:37], v[78:79] op_sel_hi:[1,0]
	v_pk_mul_f32 v[38:39], v[38:39], v[78:79] op_sel_hi:[1,0]
	v_cmp_gt_f32_e32 vcc, s26, v76
	s_waitcnt vmcnt(7)
	v_mov_b64_e32 v[70:71], v[196:197]
	v_mov_b64_e32 v[72:73], v[198:199]
	v_pk_mul_f32 v[48:49], v[70:71], v[48:49]
	v_pk_mul_f32 v[50:51], v[72:73], v[50:51]
	v_cvt_pk_bf16_f32 v48, v48, v49
	v_cvt_pk_bf16_f32 v49, v50, v51
	global_store_dwordx2 v[74:75], v[48:49], off
	s_waitcnt vmcnt(7)
	v_mov_b64_e32 v[48:49], v[200:201]
	v_mov_b64_e32 v[50:51], v[202:203]
	v_pk_mul_f32 v[48:49], v[48:49], v[52:53]
	v_pk_mul_f32 v[50:51], v[50:51], v[54:55]
	v_cvt_pk_bf16_f32 v48, v48, v49
	v_cvt_pk_bf16_f32 v49, v50, v51
	global_store_dwordx2 v[74:75], v[48:49], off offset:16
	v_pk_mul_f32 v[52:53], v[56:57], v[78:79] op_sel_hi:[1,0]
	v_pk_mul_f32 v[54:55], v[58:59], v[78:79] op_sel_hi:[1,0]
	s_waitcnt vmcnt(7)
	v_mov_b64_e32 v[48:49], v[204:205]
	v_mov_b64_e32 v[50:51], v[206:207]
	v_pk_mul_f32 v[48:49], v[48:49], v[52:53]
	v_pk_mul_f32 v[50:51], v[50:51], v[54:55]
	v_cvt_pk_bf16_f32 v48, v48, v49
	v_cvt_pk_bf16_f32 v49, v50, v51
	global_store_dwordx2 v[74:75], v[48:49], off offset:32
	v_pk_mul_f32 v[52:53], v[60:61], v[78:79] op_sel_hi:[1,0]
	v_pk_mul_f32 v[54:55], v[62:63], v[78:79] op_sel_hi:[1,0]
	s_waitcnt vmcnt(7)
	v_mov_b64_e32 v[48:49], v[208:209]
	v_mov_b64_e32 v[50:51], v[210:211]
	v_pk_mul_f32 v[48:49], v[48:49], v[52:53]
	v_pk_mul_f32 v[50:51], v[50:51], v[54:55]
	v_cvt_pk_bf16_f32 v48, v48, v49
	v_cvt_pk_bf16_f32 v49, v50, v51
	global_store_dwordx2 v[74:75], v[48:49], off offset:48
	s_waitcnt vmcnt(7)
	v_mov_b64_e32 v[48:49], v[212:213]
	v_mov_b64_e32 v[50:51], v[214:215]
	v_pk_mul_f32 v[32:33], v[32:33], v[48:49]
	v_pk_mul_f32 v[34:35], v[34:35], v[50:51]
	v_cvt_pk_bf16_f32 v32, v32, v33
	v_cvt_pk_bf16_f32 v33, v34, v35
	global_store_dwordx2 v[74:75], v[32:33], off offset:64
	s_waitcnt vmcnt(7)
; __device__ __forceinline__ unsigned cvt_pk_bf16(float lo, float hi) { typedef __bf16 bf16x2_t __attribute__((ext_vector_type(2))); f32x2 v = {lo, hi}; bf16x2_t b = __builtin_convertvector(v, bf16x2_t); return __builtin_bit_cast(unsigned, b); }
; __device__ __forceinline__ void s5_final_chunk(const Frame& F, const unsigned char* tab, const bf16* __restrict__ proj, f32x2* E, const bf16* __restrict__ wglu_t, const float* mixg, bf16* mix, int c) {
;     ...
;     for (int tt = 0; tt < 2; ++tt) { const int t = 32 * tt + r32; float tot = 0.f;
; #pragma unroll
;         for (int ww = 0; ww < 8; ++ww) tot += red[ww * 64 + t];
;         const float rstd = rsqrtf(tot * (1.0f / 512.0f) + EPS);
;         bf16* orow = mix + (size_t)(64 * c + t) * D;
; #pragma unroll
;         for (int nt = 0; nt < 2; ++nt)
; #pragma unroll
;             for (int rq = 0; rq < 4; ++rq) { const int n4 = n0 + 32 * nt + 8 * rq + 4 * hi; const f32x4 gq = *(const f32x4*)(mixg + n4);
;                 u32x2 wv; wv.x = gm::cvt_pk_bf16(z[nt][tt][4 * rq + 0] * rstd * gq.x, z[nt][tt][4 * rq + 1] * rstd * gq.y); wv.y = gm::cvt_pk_bf16(z[nt][tt][4 * rq + 2] * rstd * gq.z, z[nt][tt][4 * rq + 3] * rstd * gq.w);
;                 *(u32x2*)(orow + n4) = wv; } }
	v_mov_b64_e32 v[32:33], v[216:217]
	v_mov_b64_e32 v[34:35], v[218:219]
	v_pk_mul_f32 v[32:33], v[36:37], v[32:33]
	v_pk_mul_f32 v[34:35], v[38:39], v[34:35]
	v_cvt_pk_bf16_f32 v32, v32, v33
	v_cvt_pk_bf16_f32 v33, v34, v35
	global_store_dwordx2 v[74:75], v[32:33], off offset:80
	v_pk_mul_f32 v[36:37], v[40:41], v[78:79] op_sel_hi:[1,0]
	v_pk_mul_f32 v[38:39], v[42:43], v[78:79] op_sel_hi:[1,0]
	s_waitcnt vmcnt(7)
	v_mov_b64_e32 v[32:33], v[220:221]
	v_mov_b64_e32 v[34:35], v[222:223]
	v_pk_mul_f32 v[32:33], v[36:37], v[32:33]
	v_pk_mul_f32 v[34:35], v[38:39], v[34:35]
	v_cvt_pk_bf16_f32 v32, v32, v33
	v_cvt_pk_bf16_f32 v33, v34, v35
	global_store_dwordx2 v[74:75], v[32:33], off offset:96
	v_pk_mul_f32 v[36:37], v[44:45], v[78:79] op_sel_hi:[1,0]
	v_pk_mul_f32 v[38:39], v[46:47], v[78:79] op_sel_hi:[1,0]
	s_waitcnt vmcnt(7)
	v_mov_b64_e32 v[32:33], v[224:225]
	v_mov_b64_e32 v[34:35], v[226:227]
	v_pk_mul_f32 v[32:33], v[36:37], v[32:33]
	v_pk_mul_f32 v[34:35], v[38:39], v[34:35]
	v_cvt_pk_bf16_f32 v32, v32, v33
	v_cvt_pk_bf16_f32 v33, v34, v35
	global_store_dwordx2 v[74:75], v[32:33], off offset:112
	v_mul_f32_e32 v38, 0x4b800000, v76
	v_cndmask_b32_e32 v38, v76, v38, vcc
	v_rsq_f32_e32 v38, v38
	v_or_b32_e32 v36, s5, v68
	v_ashrrev_i32_e32 v37, 31, v36
	v_lshlrev_b64 v[36:37], 12, v[36:37]
	v_mul_f32_e32 v39, 0x45800000, v38
	v_cndmask_b32_e32 v38, v38, v39, vcc
	v_pk_mul_f32 v[16:17], v[16:17], v[38:39] op_sel_hi:[1,0]
	v_pk_mul_f32 v[18:19], v[18:19], v[38:39] op_sel_hi:[1,0]
	v_lshl_add_u64 v[36:37], s[46:47], 0, v[36:37]
	v_lshl_add_u64 v[36:37], v[36:37], 0, v[66:67]
	v_pk_mul_f32 v[20:21], v[20:21], v[38:39] op_sel_hi:[1,0]
	v_pk_mul_f32 v[22:23], v[22:23], v[38:39] op_sel_hi:[1,0]
	v_pk_mul_f32 v[0:1], v[0:1], v[38:39] op_sel_hi:[1,0]
	v_pk_mul_f32 v[2:3], v[2:3], v[38:39] op_sel_hi:[1,0]
	v_pk_mul_f32 v[4:5], v[4:5], v[38:39] op_sel_hi:[1,0]
	v_pk_mul_f32 v[6:7], v[6:7], v[38:39] op_sel_hi:[1,0]
	v_mov_b64_e32 v[32:33], v[196:197]
	v_mov_b64_e32 v[34:35], v[198:199]
	v_pk_mul_f32 v[16:17], v[32:33], v[16:17]
	v_pk_mul_f32 v[18:19], v[34:35], v[18:19]
	v_cvt_pk_bf16_f32 v16, v16, v17
	v_cvt_pk_bf16_f32 v17, v18, v19
	global_store_dwordx2 v[36:37], v[16:17], off
	v_mov_b64_e32 v[16:17], v[200:201]
	v_mov_b64_e32 v[18:19], v[202:203]
	v_pk_mul_f32 v[16:17], v[16:17], v[20:21]
	v_pk_mul_f32 v[18:19], v[18:19], v[22:23]
	v_cvt_pk_bf16_f32 v16, v16, v17
	v_cvt_pk_bf16_f32 v17, v18, v19
	global_store_dwordx2 v[36:37], v[16:17], off offset:16
	v_pk_mul_f32 v[20:21], v[24:25], v[38:39] op_sel_hi:[1,0]
	v_pk_mul_f32 v[22:23], v[26:27], v[38:39] op_sel_hi:[1,0]
	v_mov_b64_e32 v[16:17], v[204:205]
	v_mov_b64_e32 v[18:19], v[206:207]
	v_pk_mul_f32 v[16:17], v[16:17], v[20:21]
	v_pk_mul_f32 v[18:19], v[18:19], v[22:23]
	v_cvt_pk_bf16_f32 v16, v16, v17
	v_cvt_pk_bf16_f32 v17, v18, v19
	global_store_dwordx2 v[36:37], v[16:17], off offset:32
	v_pk_mul_f32 v[20:21], v[28:29], v[38:39] op_sel_hi:[1,0]
	v_pk_mul_f32 v[22:23], v[30:31], v[38:39] op_sel_hi:[1,0]
	v_mov_b64_e32 v[16:17], v[208:209]
	v_mov_b64_e32 v[18:19], v[210:211]
	v_pk_mul_f32 v[16:17], v[16:17], v[20:21]
	v_pk_mul_f32 v[18:19], v[18:19], v[22:23]
	v_cvt_pk_bf16_f32 v16, v16, v17
	v_cvt_pk_bf16_f32 v17, v18, v19
	global_store_dwordx2 v[36:37], v[16:17], off offset:48
	v_mov_b64_e32 v[16:17], v[212:213]
	v_mov_b64_e32 v[18:19], v[214:215]
	v_pk_mul_f32 v[0:1], v[0:1], v[16:17]
	v_pk_mul_f32 v[2:3], v[2:3], v[18:19]
	v_cvt_pk_bf16_f32 v0, v0, v1
	v_cvt_pk_bf16_f32 v1, v2, v3
	global_store_dwordx2 v[36:37], v[0:1], off offset:64
	v_mov_b64_e32 v[0:1], v[216:217]
	v_mov_b64_e32 v[2:3], v[218:219]
	v_pk_mul_f32 v[0:1], v[4:5], v[0:1]
	v_pk_mul_f32 v[2:3], v[6:7], v[2:3]
	v_cvt_pk_bf16_f32 v0, v0, v1
	v_cvt_pk_bf16_f32 v1, v2, v3
	global_store_dwordx2 v[36:37], v[0:1], off offset:80
	v_pk_mul_f32 v[4:5], v[8:9], v[38:39] op_sel_hi:[1,0]
	v_pk_mul_f32 v[6:7], v[10:11], v[38:39] op_sel_hi:[1,0]
	v_mov_b64_e32 v[0:1], v[220:221]
	v_mov_b64_e32 v[2:3], v[222:223]
	v_pk_mul_f32 v[0:1], v[4:5], v[0:1]
	v_pk_mul_f32 v[2:3], v[6:7], v[2:3]
	v_cvt_pk_bf16_f32 v0, v0, v1
	v_cvt_pk_bf16_f32 v1, v2, v3
	global_store_dwordx2 v[36:37], v[0:1], off offset:96
	v_pk_mul_f32 v[4:5], v[12:13], v[38:39] op_sel_hi:[1,0]
	v_pk_mul_f32 v[6:7], v[14:15], v[38:39] op_sel_hi:[1,0]
	v_mov_b64_e32 v[0:1], v[224:225]
	v_mov_b64_e32 v[2:3], v[226:227]
	v_pk_mul_f32 v[0:1], v[4:5], v[0:1]
	v_pk_mul_f32 v[2:3], v[6:7], v[2:3]
	v_cvt_pk_bf16_f32 v0, v0, v1
	v_cvt_pk_bf16_f32 v1, v2, v3
	global_store_dwordx2 v[36:37], v[0:1], off offset:112
	s_barrier
	s_cbranch_scc1 .LBB0_662
